# grid-barrier spin loops poll less often (s_sleep 1 -> s_sleep 6 between polls)
# baseline (speedup 1.0000x reference)
; __device__ __forceinline__ unsigned xb_ld(unsigned* p)              { return __hip_atomic_load(p, __ATOMIC_RELAXED, __HIP_MEMORY_SCOPE_AGENT); }
; __device__ __forceinline__ void xcd_barrier_complete(unsigned* bar, unsigned x, unsigned& nloc, unsigned& nx) {
;     const unsigned G = gridDim.x * gridDim.y * gridDim.z;
;     unsigned sum, cnt, mine, sp = 0u;
;     for (;;) {
;         sum = 0u; cnt = 0u; mine = 0u;
; #pragma unroll
;         for (unsigned j = 0; j < 16; ++j) { const unsigned c = xb_ld(&bar[XB_XCNT(j)]); sum += c; cnt += (c > 0u) ? 1u : 0u; mine = (j == x) ? c : mine; }
;         if (sum == G) break;
;         __builtin_amdgcn_s_sleep(1);
;         if ((++sp & 255u) == 0u) { if (xb_ld(&bar[XB_TMO])) break; if (sp > XB_SPIN_CAP) { atomicAdd(&bar[XB_TMO], 1u); break; } }
;     }
;     nloc = mine > 0u ? mine : 1u; nx = cnt > 0u ? cnt : 1u;
; }
.LBB0_100:
	global_load_dword v16, v17, s[8:9] sc1
	global_load_dword v1, v17, s[10:11] sc1
	global_load_dword v2, v17, s[12:13] sc1
	global_load_dword v3, v17, s[14:15] sc1
	global_load_dword v4, v17, s[16:17] sc1
	global_load_dword v5, v17, s[18:19] sc1
	global_load_dword v6, v17, s[20:21] sc1
	global_load_dword v7, v17, s[22:23] sc1
	global_load_dword v8, v17, s[24:25] sc1
	global_load_dword v9, v17, s[26:27] sc1
	global_load_dword v10, v17, s[28:29] sc1
	global_load_dword v11, v17, s[30:31] sc1
	global_load_dword v12, v17, s[34:35] sc1
	global_load_dword v13, v17, s[36:37] sc1
	global_load_dword v14, v17, s[38:39] sc1
	global_load_dword v15, v17, s[40:41] sc1
	s_mov_b64 s[42:43], -1
	s_mov_b64 s[44:45], -1
	s_waitcnt vmcnt(14)
	v_add_u32_e32 v18, v1, v16
	s_waitcnt vmcnt(13)
	v_add_u32_e32 v18, v18, v2
	s_waitcnt vmcnt(12)
	v_add_u32_e32 v18, v18, v3
	s_waitcnt vmcnt(11)
	v_add_u32_e32 v18, v18, v4
	s_waitcnt vmcnt(10)
	v_add_u32_e32 v18, v18, v5
	s_waitcnt vmcnt(9)
	v_add_u32_e32 v18, v18, v6
	s_waitcnt vmcnt(8)
	v_add_u32_e32 v18, v18, v7
	s_waitcnt vmcnt(7)
	v_add_u32_e32 v18, v18, v8
	s_waitcnt vmcnt(6)
	v_add_u32_e32 v18, v18, v9
	s_waitcnt vmcnt(5)
	v_add_u32_e32 v18, v18, v10
	s_waitcnt vmcnt(4)
	v_add_u32_e32 v18, v18, v11
	s_waitcnt vmcnt(3)
	v_add_u32_e32 v18, v18, v12
	s_waitcnt vmcnt(2)
	v_add_u32_e32 v18, v18, v13
	s_waitcnt vmcnt(1)
	v_add_u32_e32 v18, v18, v14
	s_waitcnt vmcnt(0)
	v_add_u32_e32 v18, v18, v15
	v_cmp_eq_u32_e32 vcc, s33, v18
	s_cbranch_vccnz .LBB0_99
	s_and_b32 s42, s48, 0xff
	s_cmp_eq_u32 s42, 0
	s_mov_b64 s[42:43], -1
	s_mov_b64 s[46:47], -1
	s_sleep 6
	s_cbranch_scc0 .LBB0_104
	global_load_dword v18, v17, s[6:7] sc1
	s_waitcnt vmcnt(0)
	v_cmp_eq_u32_e32 vcc, 0, v18
	s_cbranch_vccnz .LBB0_106
	s_mov_b64 s[46:47], 0

; __device__ __forceinline__ unsigned xb_ld(unsigned* p)              { return __hip_atomic_load(p, __ATOMIC_RELAXED, __HIP_MEMORY_SCOPE_AGENT); }
; __device__ __forceinline__ unsigned xb_add(unsigned* p, unsigned v) { return __hip_atomic_fetch_add(p, v, __ATOMIC_RELAXED, __HIP_MEMORY_SCOPE_AGENT); }
; #define XB_SPIN(cond, bar) do { unsigned _sp = 0; while (cond) { __builtin_amdgcn_s_sleep(1); \
;     if ((++_sp & 255u) == 0u) { if (xb_ld(&(bar)[XB_TMO])) break; if (_sp > XB_SPIN_CAP) { atomicAdd(&(bar)[XB_TMO], 1u); break; } } } } while (0)
; __device__ __forceinline__ void xcd_barrier(const XcdBarrier& b) {
;     ...
;             else XB_SPIN(xb_ld(&bar[XB_TOPGEN]) == tg, bar);
;             __builtin_amdgcn_fence(__ATOMIC_ACQUIRE, "agent");
;             xb_add(&bar[XB_XGEN(b.x)], 1u);
;             asm volatile("s_waitcnt vmcnt(0)" ::: "memory");
;         } else {
;             XB_SPIN(xb_ld(&bar[XB_XGEN(b.x)]) == gen, bar);
.LBB0_116:
	s_and_b32 s20, s24, 0xff
	s_mov_b64 s[18:19], -1
	s_cmp_lg_u32 s20, 0
	s_mov_b64 s[22:23], -1
	s_sleep 6
	s_cbranch_scc1 .LBB0_119
	global_load_dword v3, v1, s[6:7] sc1
	s_waitcnt vmcnt(0)
	v_cmp_eq_u32_e32 vcc, 0, v3
	s_cbranch_vccnz .LBB0_121
	s_mov_b64 s[22:23], 0
	s_mov_b64 s[20:21], -1

; __device__ __forceinline__ unsigned xb_ld(unsigned* p)              { return __hip_atomic_load(p, __ATOMIC_RELAXED, __HIP_MEMORY_SCOPE_AGENT); }
; __device__ __forceinline__ unsigned xb_add(unsigned* p, unsigned v) { return __hip_atomic_fetch_add(p, v, __ATOMIC_RELAXED, __HIP_MEMORY_SCOPE_AGENT); }
; #define XB_SPIN(cond, bar) do { unsigned _sp = 0; while (cond) { __builtin_amdgcn_s_sleep(1); \
;     if ((++_sp & 255u) == 0u) { if (xb_ld(&(bar)[XB_TMO])) break; if (_sp > XB_SPIN_CAP) { atomicAdd(&(bar)[XB_TMO], 1u); break; } } } } while (0)
; __device__ __forceinline__ void xcd_barrier(const XcdBarrier& b) {
;     ...
;             else XB_SPIN(xb_ld(&bar[XB_TOPGEN]) == tg, bar);
;             __builtin_amdgcn_fence(__ATOMIC_ACQUIRE, "agent");
;             xb_add(&bar[XB_XGEN(b.x)], 1u);
;             asm volatile("s_waitcnt vmcnt(0)" ::: "memory");
;         } else {
;             XB_SPIN(xb_ld(&bar[XB_XGEN(b.x)]) == gen, bar);
.LBB0_133:
	s_and_b32 s20, s26, 0xff
	s_cmp_lg_u32 s20, 0
	s_mov_b64 s[22:23], -1
	s_sleep 6
	s_cbranch_scc1 .LBB0_136
	global_load_dword v2, v1, s[6:7] sc1
	s_waitcnt vmcnt(0)
	v_cmp_eq_u32_e32 vcc, 0, v2
	s_cbranch_vccnz .LBB0_138
	s_mov_b64 s[22:23], 0
	s_mov_b64 s[20:21], -1

; __device__ __forceinline__ unsigned xb_ld(unsigned* p)              { return __hip_atomic_load(p, __ATOMIC_RELAXED, __HIP_MEMORY_SCOPE_AGENT); }
; __device__ __forceinline__ void xcd_barrier_complete(unsigned* bar, unsigned x, unsigned& nloc, unsigned& nx) {
;     const unsigned G = gridDim.x * gridDim.y * gridDim.z;
;     unsigned sum, cnt, mine, sp = 0u;
;     for (;;) {
;         sum = 0u; cnt = 0u; mine = 0u;
; #pragma unroll
;         for (unsigned j = 0; j < 16; ++j) { const unsigned c = xb_ld(&bar[XB_XCNT(j)]); sum += c; cnt += (c > 0u) ? 1u : 0u; mine = (j == x) ? c : mine; }
;         if (sum == G) break;
;         __builtin_amdgcn_s_sleep(1);
;         if ((++sp & 255u) == 0u) { if (xb_ld(&bar[XB_TMO])) break; if (sp > XB_SPIN_CAP) { atomicAdd(&bar[XB_TMO], 1u); break; } }
;     }
;     nloc = mine > 0u ? mine : 1u; nx = cnt > 0u ? cnt : 1u;
; }
.LBB0_243:
	global_load_dword v16, v17, s[4:5] sc1
	global_load_dword v1, v17, s[6:7] sc1
	global_load_dword v2, v17, s[8:9] sc1
	global_load_dword v3, v17, s[10:11] sc1
	global_load_dword v4, v17, s[12:13] sc1
	global_load_dword v5, v17, s[14:15] sc1
	global_load_dword v6, v17, s[16:17] sc1
	global_load_dword v7, v17, s[18:19] sc1
	global_load_dword v8, v17, s[20:21] sc1
	global_load_dword v9, v17, s[22:23] sc1
	global_load_dword v10, v17, s[24:25] sc1
	global_load_dword v11, v17, s[26:27] sc1
	global_load_dword v12, v17, s[28:29] sc1
	global_load_dword v13, v17, s[30:31] sc1
	global_load_dword v14, v17, s[34:35] sc1
	global_load_dword v15, v17, s[36:37] sc1
	s_mov_b64 s[38:39], -1
	s_mov_b64 s[40:41], -1
	s_waitcnt vmcnt(14)
	v_add_u32_e32 v18, v1, v16
	s_waitcnt vmcnt(13)
	v_add_u32_e32 v18, v18, v2
	s_waitcnt vmcnt(12)
	v_add_u32_e32 v18, v18, v3
	s_waitcnt vmcnt(11)
	v_add_u32_e32 v18, v18, v4
	s_waitcnt vmcnt(10)
	v_add_u32_e32 v18, v18, v5
	s_waitcnt vmcnt(9)
	v_add_u32_e32 v18, v18, v6
	s_waitcnt vmcnt(8)
	v_add_u32_e32 v18, v18, v7
	s_waitcnt vmcnt(7)
	v_add_u32_e32 v18, v18, v8
	s_waitcnt vmcnt(6)
	v_add_u32_e32 v18, v18, v9
	s_waitcnt vmcnt(5)
	v_add_u32_e32 v18, v18, v10
	s_waitcnt vmcnt(4)
	v_add_u32_e32 v18, v18, v11
	s_waitcnt vmcnt(3)
	v_add_u32_e32 v18, v18, v12
	s_waitcnt vmcnt(2)
	v_add_u32_e32 v18, v18, v13
	s_waitcnt vmcnt(1)
	v_add_u32_e32 v18, v18, v14
	s_waitcnt vmcnt(0)
	v_add_u32_e32 v18, v18, v15
	v_cmp_eq_u32_e32 vcc, s33, v18
	s_cbranch_vccnz .LBB0_242
	s_and_b32 s38, s44, 0xff
	s_cmp_eq_u32 s38, 0
	s_mov_b64 s[38:39], -1
	s_mov_b64 s[42:43], -1
	s_sleep 6
	s_cbranch_scc0 .LBB0_247
	global_load_dword v18, v17, s[2:3] sc1
	s_waitcnt vmcnt(0)
	v_cmp_eq_u32_e32 vcc, 0, v18
	s_cbranch_vccnz .LBB0_249
	s_mov_b64 s[42:43], 0

; __device__ __forceinline__ unsigned xb_ld(unsigned* p)              { return __hip_atomic_load(p, __ATOMIC_RELAXED, __HIP_MEMORY_SCOPE_AGENT); }
; __device__ __forceinline__ unsigned xb_add(unsigned* p, unsigned v) { return __hip_atomic_fetch_add(p, v, __ATOMIC_RELAXED, __HIP_MEMORY_SCOPE_AGENT); }
; #define XB_SPIN(cond, bar) do { unsigned _sp = 0; while (cond) { __builtin_amdgcn_s_sleep(1); \
;     if ((++_sp & 255u) == 0u) { if (xb_ld(&(bar)[XB_TMO])) break; if (_sp > XB_SPIN_CAP) { atomicAdd(&(bar)[XB_TMO], 1u); break; } } } } while (0)
; __device__ __forceinline__ void xcd_barrier(const XcdBarrier& b) {
;     ...
;             else XB_SPIN(xb_ld(&bar[XB_TOPGEN]) == tg, bar);
;             __builtin_amdgcn_fence(__ATOMIC_ACQUIRE, "agent");
;             xb_add(&bar[XB_XGEN(b.x)], 1u);
;             asm volatile("s_waitcnt vmcnt(0)" ::: "memory");
;         } else {
;             XB_SPIN(xb_ld(&bar[XB_XGEN(b.x)]) == gen, bar);
.LBB0_259:
	s_and_b32 s16, s20, 0xff
	s_mov_b64 s[14:15], -1
	s_cmp_lg_u32 s16, 0
	s_mov_b64 s[18:19], -1
	s_sleep 6
	s_cbranch_scc1 .LBB0_262
	global_load_dword v3, v1, s[2:3] sc1
	s_waitcnt vmcnt(0)
	v_cmp_eq_u32_e32 vcc, 0, v3
	s_cbranch_vccnz .LBB0_264
	s_mov_b64 s[18:19], 0
	s_mov_b64 s[16:17], -1

; __device__ __forceinline__ unsigned xb_ld(unsigned* p)              { return __hip_atomic_load(p, __ATOMIC_RELAXED, __HIP_MEMORY_SCOPE_AGENT); }
; __device__ __forceinline__ unsigned xb_add(unsigned* p, unsigned v) { return __hip_atomic_fetch_add(p, v, __ATOMIC_RELAXED, __HIP_MEMORY_SCOPE_AGENT); }
; #define XB_SPIN(cond, bar) do { unsigned _sp = 0; while (cond) { __builtin_amdgcn_s_sleep(1); \
;     if ((++_sp & 255u) == 0u) { if (xb_ld(&(bar)[XB_TMO])) break; if (_sp > XB_SPIN_CAP) { atomicAdd(&(bar)[XB_TMO], 1u); break; } } } } while (0)
; __device__ __forceinline__ void xcd_barrier(const XcdBarrier& b) {
;     ...
;             else XB_SPIN(xb_ld(&bar[XB_TOPGEN]) == tg, bar);
;             __builtin_amdgcn_fence(__ATOMIC_ACQUIRE, "agent");
;             xb_add(&bar[XB_XGEN(b.x)], 1u);
;             asm volatile("s_waitcnt vmcnt(0)" ::: "memory");
;         } else {
;             XB_SPIN(xb_ld(&bar[XB_XGEN(b.x)]) == gen, bar);
.LBB0_276:
	s_and_b32 s16, s22, 0xff
	s_cmp_lg_u32 s16, 0
	s_mov_b64 s[18:19], -1
	s_sleep 6
	s_cbranch_scc1 .LBB0_279
	global_load_dword v2, v1, s[2:3] sc1
	s_waitcnt vmcnt(0)
	v_cmp_eq_u32_e32 vcc, 0, v2
	s_cbranch_vccnz .LBB0_281
	s_mov_b64 s[18:19], 0
	s_mov_b64 s[16:17], -1

; __device__ __forceinline__ unsigned xb_ld(unsigned* p)              { return __hip_atomic_load(p, __ATOMIC_RELAXED, __HIP_MEMORY_SCOPE_AGENT); }
; __device__ __forceinline__ void xcd_barrier_complete(unsigned* bar, unsigned x, unsigned& nloc, unsigned& nx) {
;     const unsigned G = gridDim.x * gridDim.y * gridDim.z;
;     unsigned sum, cnt, mine, sp = 0u;
;     for (;;) {
;         sum = 0u; cnt = 0u; mine = 0u;
; #pragma unroll
;         for (unsigned j = 0; j < 16; ++j) { const unsigned c = xb_ld(&bar[XB_XCNT(j)]); sum += c; cnt += (c > 0u) ? 1u : 0u; mine = (j == x) ? c : mine; }
;         if (sum == G) break;
;         __builtin_amdgcn_s_sleep(1);
;         if ((++sp & 255u) == 0u) { if (xb_ld(&bar[XB_TMO])) break; if (sp > XB_SPIN_CAP) { atomicAdd(&bar[XB_TMO], 1u); break; } }
;     }
;     nloc = mine > 0u ? mine : 1u; nx = cnt > 0u ? cnt : 1u;
; }
.LBB0_937:
	global_load_dword v16, v17, s[4:5] sc1
	global_load_dword v1, v17, s[6:7] sc1
	global_load_dword v2, v17, s[8:9] sc1
	global_load_dword v3, v17, s[10:11] sc1
	global_load_dword v4, v17, s[12:13] sc1
	global_load_dword v5, v17, s[14:15] sc1
	global_load_dword v6, v17, s[16:17] sc1
	global_load_dword v7, v17, s[20:21] sc1
	global_load_dword v8, v17, s[22:23] sc1
	global_load_dword v9, v17, s[24:25] sc1
	global_load_dword v10, v17, s[26:27] sc1
	global_load_dword v11, v17, s[28:29] sc1
	global_load_dword v12, v17, s[30:31] sc1
	global_load_dword v13, v17, s[34:35] sc1
	global_load_dword v14, v17, s[36:37] sc1
	global_load_dword v15, v17, s[38:39] sc1
	s_mov_b64 s[40:41], -1
	s_mov_b64 s[42:43], -1
	s_waitcnt vmcnt(14)
	v_add_u32_e32 v18, v1, v16
	s_waitcnt vmcnt(13)
	v_add_u32_e32 v18, v18, v2
	s_waitcnt vmcnt(12)
	v_add_u32_e32 v18, v18, v3
	s_waitcnt vmcnt(11)
	v_add_u32_e32 v18, v18, v4
	s_waitcnt vmcnt(10)
	v_add_u32_e32 v18, v18, v5
	s_waitcnt vmcnt(9)
	v_add_u32_e32 v18, v18, v6
	s_waitcnt vmcnt(8)
	v_add_u32_e32 v18, v18, v7
	s_waitcnt vmcnt(7)
	v_add_u32_e32 v18, v18, v8
	s_waitcnt vmcnt(6)
	v_add_u32_e32 v18, v18, v9
	s_waitcnt vmcnt(5)
	v_add_u32_e32 v18, v18, v10
	s_waitcnt vmcnt(4)
	v_add_u32_e32 v18, v18, v11
	s_waitcnt vmcnt(3)
	v_add_u32_e32 v18, v18, v12
	s_waitcnt vmcnt(2)
	v_add_u32_e32 v18, v18, v13
	s_waitcnt vmcnt(1)
	v_add_u32_e32 v18, v18, v14
	s_waitcnt vmcnt(0)
	v_add_u32_e32 v18, v18, v15
	v_cmp_eq_u32_e32 vcc, s33, v18
	s_cbranch_vccnz .LBB0_936
	s_and_b32 s40, s46, 0xff
	s_cmp_eq_u32 s40, 0
	s_mov_b64 s[40:41], -1
	s_mov_b64 s[44:45], -1
	s_sleep 6
	s_cbranch_scc0 .LBB0_941
	global_load_dword v18, v17, s[2:3] sc1
	s_waitcnt vmcnt(0)
	v_cmp_eq_u32_e32 vcc, 0, v18
	s_cbranch_vccnz .LBB0_943
	s_mov_b64 s[44:45], 0

; __device__ __forceinline__ unsigned xb_ld(unsigned* p)              { return __hip_atomic_load(p, __ATOMIC_RELAXED, __HIP_MEMORY_SCOPE_AGENT); }
; __device__ __forceinline__ unsigned xb_add(unsigned* p, unsigned v) { return __hip_atomic_fetch_add(p, v, __ATOMIC_RELAXED, __HIP_MEMORY_SCOPE_AGENT); }
; #define XB_SPIN(cond, bar) do { unsigned _sp = 0; while (cond) { __builtin_amdgcn_s_sleep(1); \
;     if ((++_sp & 255u) == 0u) { if (xb_ld(&(bar)[XB_TMO])) break; if (_sp > XB_SPIN_CAP) { atomicAdd(&(bar)[XB_TMO], 1u); break; } } } } while (0)
; __device__ __forceinline__ void xcd_barrier(const XcdBarrier& b) {
;     ...
;             else XB_SPIN(xb_ld(&bar[XB_TOPGEN]) == tg, bar);
;             __builtin_amdgcn_fence(__ATOMIC_ACQUIRE, "agent");
;             xb_add(&bar[XB_XGEN(b.x)], 1u);
;             asm volatile("s_waitcnt vmcnt(0)" ::: "memory");
;         } else {
;             XB_SPIN(xb_ld(&bar[XB_XGEN(b.x)]) == gen, bar);
.LBB0_953:
	s_and_b32 s16, s22, 0xff
	s_mov_b64 s[14:15], -1
	s_cmp_lg_u32 s16, 0
	s_mov_b64 s[20:21], -1
	s_sleep 6
	s_cbranch_scc1 .LBB0_956
	global_load_dword v3, v1, s[2:3] sc1
	s_waitcnt vmcnt(0)
	v_cmp_eq_u32_e32 vcc, 0, v3
	s_cbranch_vccnz .LBB0_958
	s_mov_b64 s[20:21], 0
	s_mov_b64 s[16:17], -1

; __device__ __forceinline__ unsigned xb_ld(unsigned* p)              { return __hip_atomic_load(p, __ATOMIC_RELAXED, __HIP_MEMORY_SCOPE_AGENT); }
; __device__ __forceinline__ unsigned xb_add(unsigned* p, unsigned v) { return __hip_atomic_fetch_add(p, v, __ATOMIC_RELAXED, __HIP_MEMORY_SCOPE_AGENT); }
; #define XB_SPIN(cond, bar) do { unsigned _sp = 0; while (cond) { __builtin_amdgcn_s_sleep(1); \
;     if ((++_sp & 255u) == 0u) { if (xb_ld(&(bar)[XB_TMO])) break; if (_sp > XB_SPIN_CAP) { atomicAdd(&(bar)[XB_TMO], 1u); break; } } } } while (0)
; __device__ __forceinline__ void xcd_barrier(const XcdBarrier& b) {
;     ...
;             else XB_SPIN(xb_ld(&bar[XB_TOPGEN]) == tg, bar);
;             __builtin_amdgcn_fence(__ATOMIC_ACQUIRE, "agent");
;             xb_add(&bar[XB_XGEN(b.x)], 1u);
;             asm volatile("s_waitcnt vmcnt(0)" ::: "memory");
;         } else {
;             XB_SPIN(xb_ld(&bar[XB_XGEN(b.x)]) == gen, bar);
.LBB0_970:
	s_and_b32 s16, s24, 0xff
	s_cmp_lg_u32 s16, 0
	s_mov_b64 s[20:21], -1
	s_sleep 6
	s_cbranch_scc1 .LBB0_973
	global_load_dword v2, v1, s[2:3] sc1
	s_waitcnt vmcnt(0)
	v_cmp_eq_u32_e32 vcc, 0, v2
	s_cbranch_vccnz .LBB0_975
	s_mov_b64 s[20:21], 0
	s_mov_b64 s[16:17], -1

; __device__ __forceinline__ unsigned xb_ld(unsigned* p)              { return __hip_atomic_load(p, __ATOMIC_RELAXED, __HIP_MEMORY_SCOPE_AGENT); }
; __device__ __forceinline__ void xcd_barrier_complete(unsigned* bar, unsigned x, unsigned& nloc, unsigned& nx) {
;     const unsigned G = gridDim.x * gridDim.y * gridDim.z;
;     unsigned sum, cnt, mine, sp = 0u;
;     for (;;) {
;         sum = 0u; cnt = 0u; mine = 0u;
; #pragma unroll
;         for (unsigned j = 0; j < 16; ++j) { const unsigned c = xb_ld(&bar[XB_XCNT(j)]); sum += c; cnt += (c > 0u) ? 1u : 0u; mine = (j == x) ? c : mine; }
;         if (sum == G) break;
;         __builtin_amdgcn_s_sleep(1);
;         if ((++sp & 255u) == 0u) { if (xb_ld(&bar[XB_TMO])) break; if (sp > XB_SPIN_CAP) { atomicAdd(&bar[XB_TMO], 1u); break; } }
;     }
;     nloc = mine > 0u ? mine : 1u; nx = cnt > 0u ? cnt : 1u;
; }
.LBB0_1467:
	global_load_dword v16, v17, s[22:23] sc1
	global_load_dword v1, v17, s[4:5] sc1
	global_load_dword v2, v17, s[24:25] sc1
	global_load_dword v3, v17, s[6:7] sc1
	global_load_dword v4, v17, s[26:27] sc1
	global_load_dword v5, v17, s[8:9] sc1
	global_load_dword v6, v17, s[28:29] sc1
	global_load_dword v7, v17, s[10:11] sc1
	global_load_dword v8, v17, s[30:31] sc1
	global_load_dword v9, v17, s[12:13] sc1
	global_load_dword v10, v17, s[34:35] sc1
	global_load_dword v11, v17, s[14:15] sc1
	global_load_dword v12, v17, s[36:37] sc1
	global_load_dword v13, v17, s[16:17] sc1
	global_load_dword v14, v17, s[38:39] sc1
	global_load_dword v15, v17, s[20:21] sc1
	s_mov_b64 s[40:41], -1
	s_mov_b64 s[42:43], -1
	s_waitcnt vmcnt(14)
	v_add_u32_e32 v18, v1, v16
	s_waitcnt vmcnt(13)
	v_add_u32_e32 v18, v18, v2
	s_waitcnt vmcnt(12)
	v_add_u32_e32 v18, v18, v3
	s_waitcnt vmcnt(11)
	v_add_u32_e32 v18, v18, v4
	s_waitcnt vmcnt(10)
	v_add_u32_e32 v18, v18, v5
	s_waitcnt vmcnt(9)
	v_add_u32_e32 v18, v18, v6
	s_waitcnt vmcnt(8)
	v_add_u32_e32 v18, v18, v7
	s_waitcnt vmcnt(7)
	v_add_u32_e32 v18, v18, v8
	s_waitcnt vmcnt(6)
	v_add_u32_e32 v18, v18, v9
	s_waitcnt vmcnt(5)
	v_add_u32_e32 v18, v18, v10
	s_waitcnt vmcnt(4)
	v_add_u32_e32 v18, v18, v11
	s_waitcnt vmcnt(3)
	v_add_u32_e32 v18, v18, v12
	s_waitcnt vmcnt(2)
	v_add_u32_e32 v18, v18, v13
	s_waitcnt vmcnt(1)
	v_add_u32_e32 v18, v18, v14
	s_waitcnt vmcnt(0)
	v_add_u32_e32 v18, v18, v15
	v_cmp_eq_u32_e32 vcc, s33, v18
	s_cbranch_vccnz .LBB0_1466
	s_and_b32 s40, s46, 0xff
	s_cmp_eq_u32 s40, 0
	s_mov_b64 s[40:41], -1
	s_mov_b64 s[44:45], -1
	s_sleep 6
	s_cbranch_scc0 .LBB0_1471
	global_load_dword v18, v17, s[2:3] sc1
	s_waitcnt vmcnt(0)
	v_cmp_eq_u32_e32 vcc, 0, v18
	s_cbranch_vccnz .LBB0_1473
	s_mov_b64 s[44:45], 0

; __device__ __forceinline__ unsigned xb_ld(unsigned* p)              { return __hip_atomic_load(p, __ATOMIC_RELAXED, __HIP_MEMORY_SCOPE_AGENT); }
; __device__ __forceinline__ unsigned xb_add(unsigned* p, unsigned v) { return __hip_atomic_fetch_add(p, v, __ATOMIC_RELAXED, __HIP_MEMORY_SCOPE_AGENT); }
; #define XB_SPIN(cond, bar) do { unsigned _sp = 0; while (cond) { __builtin_amdgcn_s_sleep(1); \
;     if ((++_sp & 255u) == 0u) { if (xb_ld(&(bar)[XB_TMO])) break; if (_sp > XB_SPIN_CAP) { atomicAdd(&(bar)[XB_TMO], 1u); break; } } } } while (0)
; __device__ __forceinline__ void xcd_barrier(const XcdBarrier& b) {
;     ...
;             else XB_SPIN(xb_ld(&bar[XB_TOPGEN]) == tg, bar);
;             __builtin_amdgcn_fence(__ATOMIC_ACQUIRE, "agent");
;             xb_add(&bar[XB_XGEN(b.x)], 1u);
;             asm volatile("s_waitcnt vmcnt(0)" ::: "memory");
;         } else {
;             XB_SPIN(xb_ld(&bar[XB_XGEN(b.x)]) == gen, bar);
.LBB0_1551:
	s_and_b32 s20, s24, 0xff
	s_mov_b64 s[16:17], -1
	s_cmp_lg_u32 s20, 0
	s_mov_b64 s[22:23], -1
	s_sleep 6
	s_cbranch_scc1 .LBB0_1554
	global_load_dword v3, v1, s[8:9] sc1
	s_waitcnt vmcnt(0)
	v_cmp_eq_u32_e32 vcc, 0, v3
	s_cbranch_vccnz .LBB0_1556
	s_mov_b64 s[22:23], 0
	s_mov_b64 s[20:21], -1

; __device__ __forceinline__ unsigned xb_ld(unsigned* p)              { return __hip_atomic_load(p, __ATOMIC_RELAXED, __HIP_MEMORY_SCOPE_AGENT); }
; __device__ __forceinline__ unsigned xb_add(unsigned* p, unsigned v) { return __hip_atomic_fetch_add(p, v, __ATOMIC_RELAXED, __HIP_MEMORY_SCOPE_AGENT); }
; #define XB_SPIN(cond, bar) do { unsigned _sp = 0; while (cond) { __builtin_amdgcn_s_sleep(1); \
;     if ((++_sp & 255u) == 0u) { if (xb_ld(&(bar)[XB_TMO])) break; if (_sp > XB_SPIN_CAP) { atomicAdd(&(bar)[XB_TMO], 1u); break; } } } } while (0)
; __device__ __forceinline__ void xcd_barrier(const XcdBarrier& b) {
;     ...
;             else XB_SPIN(xb_ld(&bar[XB_TOPGEN]) == tg, bar);
;             __builtin_amdgcn_fence(__ATOMIC_ACQUIRE, "agent");
;             xb_add(&bar[XB_XGEN(b.x)], 1u);
;             asm volatile("s_waitcnt vmcnt(0)" ::: "memory");
;         } else {
;             XB_SPIN(xb_ld(&bar[XB_XGEN(b.x)]) == gen, bar);
.LBB0_1568:
	s_and_b32 s16, s24, 0xff
	s_cmp_lg_u32 s16, 0
	s_mov_b64 s[20:21], -1
	s_sleep 6
	s_cbranch_scc1 .LBB0_1571
	global_load_dword v2, v1, s[8:9] sc1
	s_waitcnt vmcnt(0)
	v_cmp_eq_u32_e32 vcc, 0, v2
	s_cbranch_vccnz .LBB0_1573
	s_mov_b64 s[20:21], 0
	s_mov_b64 s[16:17], -1

; __device__ __forceinline__ unsigned xb_ld(unsigned* p)              { return __hip_atomic_load(p, __ATOMIC_RELAXED, __HIP_MEMORY_SCOPE_AGENT); }
; __device__ __forceinline__ void xcd_barrier_complete(unsigned* bar, unsigned x, unsigned& nloc, unsigned& nx) {
;     const unsigned G = gridDim.x * gridDim.y * gridDim.z;
;     unsigned sum, cnt, mine, sp = 0u;
;     for (;;) {
;         sum = 0u; cnt = 0u; mine = 0u;
; #pragma unroll
;         for (unsigned j = 0; j < 16; ++j) { const unsigned c = xb_ld(&bar[XB_XCNT(j)]); sum += c; cnt += (c > 0u) ? 1u : 0u; mine = (j == x) ? c : mine; }
;         if (sum == G) break;
;         __builtin_amdgcn_s_sleep(1);
;         if ((++sp & 255u) == 0u) { if (xb_ld(&bar[XB_TMO])) break; if (sp > XB_SPIN_CAP) { atomicAdd(&bar[XB_TMO], 1u); break; } }
;     }
;     nloc = mine > 0u ? mine : 1u; nx = cnt > 0u ? cnt : 1u;
; }
.LBB0_1746:
	global_load_dword v15, v16, s[4:5] sc1
	global_load_dword v0, v16, s[6:7] sc1
	global_load_dword v1, v16, s[8:9] sc1
	global_load_dword v2, v16, s[10:11] sc1
	global_load_dword v3, v16, s[12:13] sc1
	global_load_dword v4, v16, s[14:15] sc1
	global_load_dword v5, v16, s[16:17] sc1
	global_load_dword v6, v16, s[20:21] sc1
	global_load_dword v7, v16, s[22:23] sc1
	global_load_dword v8, v16, s[24:25] sc1
	global_load_dword v9, v16, s[26:27] sc1
	global_load_dword v10, v16, s[28:29] sc1
	global_load_dword v11, v16, s[30:31] sc1
	global_load_dword v12, v16, s[34:35] sc1
	global_load_dword v13, v16, s[36:37] sc1
	global_load_dword v14, v16, s[38:39] sc1
	s_mov_b64 s[40:41], -1
	s_mov_b64 s[42:43], -1
	s_waitcnt vmcnt(14)
	v_add_u32_e32 v17, v0, v15
	s_waitcnt vmcnt(13)
	v_add_u32_e32 v17, v17, v1
	s_waitcnt vmcnt(12)
	v_add_u32_e32 v17, v17, v2
	s_waitcnt vmcnt(11)
	v_add_u32_e32 v17, v17, v3
	s_waitcnt vmcnt(10)
	v_add_u32_e32 v17, v17, v4
	s_waitcnt vmcnt(9)
	v_add_u32_e32 v17, v17, v5
	s_waitcnt vmcnt(8)
	v_add_u32_e32 v17, v17, v6
	s_waitcnt vmcnt(7)
	v_add_u32_e32 v17, v17, v7
	s_waitcnt vmcnt(6)
	v_add_u32_e32 v17, v17, v8
	s_waitcnt vmcnt(5)
	v_add_u32_e32 v17, v17, v9
	s_waitcnt vmcnt(4)
	v_add_u32_e32 v17, v17, v10
	s_waitcnt vmcnt(3)
	v_add_u32_e32 v17, v17, v11
	s_waitcnt vmcnt(2)
	v_add_u32_e32 v17, v17, v12
	s_waitcnt vmcnt(1)
	v_add_u32_e32 v17, v17, v13
	s_waitcnt vmcnt(0)
	v_add_u32_e32 v17, v17, v14
	v_cmp_eq_u32_e32 vcc, s33, v17
	s_cbranch_vccnz .LBB0_1745
	s_and_b32 s40, s46, 0xff
	s_cmp_eq_u32 s40, 0
	s_mov_b64 s[40:41], -1
	s_mov_b64 s[44:45], -1
	s_sleep 6
	s_cbranch_scc0 .LBB0_1750
	global_load_dword v17, v16, s[2:3] sc1
	s_waitcnt vmcnt(0)
	v_cmp_eq_u32_e32 vcc, 0, v17
	s_cbranch_vccnz .LBB0_1752
	s_mov_b64 s[44:45], 0

; __device__ __forceinline__ unsigned xb_ld(unsigned* p)              { return __hip_atomic_load(p, __ATOMIC_RELAXED, __HIP_MEMORY_SCOPE_AGENT); }
; __device__ __forceinline__ unsigned xb_add(unsigned* p, unsigned v) { return __hip_atomic_fetch_add(p, v, __ATOMIC_RELAXED, __HIP_MEMORY_SCOPE_AGENT); }
; #define XB_SPIN(cond, bar) do { unsigned _sp = 0; while (cond) { __builtin_amdgcn_s_sleep(1); \
;     if ((++_sp & 255u) == 0u) { if (xb_ld(&(bar)[XB_TMO])) break; if (_sp > XB_SPIN_CAP) { atomicAdd(&(bar)[XB_TMO], 1u); break; } } } } while (0)
; __device__ __forceinline__ void xcd_barrier(const XcdBarrier& b) {
;     ...
;             else XB_SPIN(xb_ld(&bar[XB_TOPGEN]) == tg, bar);
;             __builtin_amdgcn_fence(__ATOMIC_ACQUIRE, "agent");
;             xb_add(&bar[XB_XGEN(b.x)], 1u);
;             asm volatile("s_waitcnt vmcnt(0)" ::: "memory");
;         } else {
;             XB_SPIN(xb_ld(&bar[XB_XGEN(b.x)]) == gen, bar);
.LBB0_1762:
	s_and_b32 s16, s22, 0xff
	s_mov_b64 s[14:15], -1
	s_cmp_lg_u32 s16, 0
	s_mov_b64 s[20:21], -1
	s_sleep 6
	s_cbranch_scc1 .LBB0_1765
	global_load_dword v2, v0, s[2:3] sc1
	s_waitcnt vmcnt(0)
	v_cmp_eq_u32_e32 vcc, 0, v2
	s_cbranch_vccnz .LBB0_1767
	s_mov_b64 s[20:21], 0
	s_mov_b64 s[16:17], -1

; __device__ __forceinline__ unsigned xb_ld(unsigned* p)              { return __hip_atomic_load(p, __ATOMIC_RELAXED, __HIP_MEMORY_SCOPE_AGENT); }
; __device__ __forceinline__ unsigned xb_add(unsigned* p, unsigned v) { return __hip_atomic_fetch_add(p, v, __ATOMIC_RELAXED, __HIP_MEMORY_SCOPE_AGENT); }
; #define XB_SPIN(cond, bar) do { unsigned _sp = 0; while (cond) { __builtin_amdgcn_s_sleep(1); \
;     if ((++_sp & 255u) == 0u) { if (xb_ld(&(bar)[XB_TMO])) break; if (_sp > XB_SPIN_CAP) { atomicAdd(&(bar)[XB_TMO], 1u); break; } } } } while (0)
; __device__ __forceinline__ void xcd_barrier(const XcdBarrier& b) {
;     ...
;             else XB_SPIN(xb_ld(&bar[XB_TOPGEN]) == tg, bar);
;             __builtin_amdgcn_fence(__ATOMIC_ACQUIRE, "agent");
;             xb_add(&bar[XB_XGEN(b.x)], 1u);
;             asm volatile("s_waitcnt vmcnt(0)" ::: "memory");
;         } else {
;             XB_SPIN(xb_ld(&bar[XB_XGEN(b.x)]) == gen, bar);
.LBB0_1779:
	s_and_b32 s16, s24, 0xff
	s_cmp_lg_u32 s16, 0
	s_mov_b64 s[20:21], -1
	s_sleep 6
	s_cbranch_scc1 .LBB0_1782
	global_load_dword v1, v0, s[2:3] sc1
	s_waitcnt vmcnt(0)
	v_cmp_eq_u32_e32 vcc, 0, v1
	s_cbranch_vccnz .LBB0_1784
	s_mov_b64 s[20:21], 0
	s_mov_b64 s[16:17], -1
